# hand-written steady-state attention tile loops: per-group loops, softmax max/exp inside the MFMA burst, DMA issue after fragment reads
# speedup vs baseline: 1.0411x; 1.0294x over previous
.LBB0_522:
	s_waitcnt lgkmcnt(0)
	s_barrier
	s_mov_b32 s13, 1
	s_mov_b32 s0, 2
	s_mov_b32 s2, 5
	s_mov_b32 s3, s61
	s_and_b64 vcc, exec, s[4:5]
	s_mov_b32 s12, s0
	s_cmp_lt_u32 s2, s16
	s_cbranch_scc0 .Lfa_none
	s_cbranch_vccnz .Lfa0_loop
	s_branch .Lfa1_entry
.Lfa_none:
	s_cbranch_vccnz .LBB0_528

.Lfa0_loop:
	s_lshl_b32 s0, s12, 12
	s_add_i32 s0, s91, s0
	s_lshl_b32 s1, s13, 13
	s_add_i32 s1, s91, s1
	v_add_u32_e32 v232, s0, v222
	v_add_u32_e32 v233, s0, v221
	v_add_u32_e32 v234, s1, v222
	v_add_u32_e32 v235, s1, v221
	ds_read_b128 v[144:147], v232
	ds_read_b128 v[148:151], v233
	ds_read_b128 v[152:155], v232 offset:2048
	ds_read_b128 v[156:159], v233 offset:2048
	ds_read_b128 v[176:179], v234 offset:16384
	ds_read_b128 v[180:183], v235 offset:16384
	ds_read_b128 v[168:171], v234 offset:18432
	ds_read_b128 v[172:175], v235 offset:18432
	ds_read_b128 v[192:195], v234 offset:20480
	ds_read_b128 v[196:199], v235 offset:20480
	ds_read_b128 v[184:187], v234 offset:22528
	ds_read_b128 v[188:191], v235 offset:22528
	s_add_i32 s10, s12, 3
	s_and_b32 s10, s10, 3
	s_add_i32 s33, s10, 3
	s_and_b32 s33, s33, 3
	s_lshl_b32 s33, s33, 13
	s_add_i32 s33, s33, s79
	s_addk_i32 s33, 0x4000
	s_add_i32 s32, s86, s2
	s_add_i32 s50, s32, -1
	s_mov_b32 s51, 0
	s_lshl_b64 s[50:51], s[50:51], 6
	s_add_u32 s50, s97, s50
	s_addc_u32 s51, s87, s51
	s_lshl_b32 s11, s10, 12
	s_add_i32 s11, s11, s79
	s_add_i32 s10, s32, -3
	s_cmp_lt_u32 s10, 61
	s_cselect_b32 s10, s90, s17
	s_add_i32 s48, s10, s3
	s_ashr_i32 s49, s48, 31
	s_lshl_b64 s[48:49], s[48:49], 10
	s_add_u32 s48, s95, s48
	s_addc_u32 s49, s96, s49
	s_mov_b32 m0, s11
	s_nop 0
	global_load_lds_dwordx4 v209, s[48:49]
	s_mov_b32 m0, s33
	s_nop 0
	global_load_lds_dwordx4 v218, s[50:51]
	s_waitcnt lgkmcnt(10)
	v_mfma_scale_f32_32x32x64_f8f6f4 v[96:111], v[144:151], v[128:135], v[80:95], v220, v220 op_sel_hi:[0,0,0]
	s_waitcnt lgkmcnt(8)
	v_mfma_scale_f32_32x32x64_f8f6f4 v[112:127], v[152:159], v[128:135], v[80:95], v220, v220 op_sel_hi:[0,0,0]
	v_mfma_scale_f32_32x32x64_f8f6f4 v[0:15], v[160:167], v[136:143], v[0:15], v219, v219 op_sel_hi:[0,0,0]
	v_max3_f32 v226, v96, v97, v98
	v_max3_f32 v202, v99, v100, v101
	v_max3_f32 v203, v102, v103, v104
	v_max3_f32 v211, v105, v106, v107
	v_max3_f32 v226, v226, v108, v109
	v_max3_f32 v202, v202, v110, v111
	v_max3_f32 v226, v226, v203, v211
	v_max_f32_e32 v226, v226, v202
	s_waitcnt lgkmcnt(6)
	v_mfma_scale_f32_32x32x64_f8f6f4 v[64:79], v[160:167], v[176:183], v[64:79], v219, v219 op_sel_hi:[0,0,0]
	v_max3_f32 v227, v112, v113, v114
	v_max3_f32 v202, v115, v116, v117
	v_max3_f32 v203, v118, v119, v120
	v_max3_f32 v211, v121, v122, v123
	v_max3_f32 v227, v227, v124, v125
	v_max3_f32 v202, v202, v126, v127
	v_max3_f32 v227, v227, v203, v211
	v_max_f32_e32 v227, v227, v202
	v_max_f32_e32 v226, v226, v227
	v_mov_b32_e32 v227, v226
	s_nop 1
	v_permlane32_swap_b32_e32 v226, v227
	v_max3_f32 v226, v226, v227, v227
	s_nop 0
	v_cmp_lt_f32_e32 vcc, 0x41000000, v226
	s_cbranch_vccnz .Lfa0_rare
	s_waitcnt lgkmcnt(4)
	v_mfma_scale_f32_32x32x64_f8f6f4 v[48:63], v[160:167], v[168:175], v[48:63], v219, v219 op_sel_hi:[0,0,0]
	v_exp_f32_e32 v96, v96
	v_exp_f32_e32 v112, v112
	v_exp_f32_e32 v97, v97
	v_exp_f32_e32 v113, v113
	v_exp_f32_e32 v100, v100
	v_exp_f32_e32 v116, v116
	v_exp_f32_e32 v101, v101
	v_exp_f32_e32 v117, v117
	s_waitcnt lgkmcnt(2)
	v_mfma_scale_f32_32x32x64_f8f6f4 v[32:47], v[160:167], v[192:199], v[32:47], v219, v219 op_sel_hi:[0,0,0]
	v_exp_f32_e32 v104, v104
	v_exp_f32_e32 v120, v120
	v_exp_f32_e32 v105, v105
	v_exp_f32_e32 v121, v121
	v_exp_f32_e32 v108, v108
	v_exp_f32_e32 v124, v124
	v_exp_f32_e32 v109, v109
	v_exp_f32_e32 v125, v125
	s_waitcnt lgkmcnt(0)
	v_mfma_scale_f32_32x32x64_f8f6f4 v[16:31], v[160:167], v[184:191], v[16:31], v219, v219 op_sel_hi:[0,0,0]
	v_exp_f32_e32 v98, v98
	v_exp_f32_e32 v114, v114
	v_exp_f32_e32 v99, v99
	v_exp_f32_e32 v115, v115
	v_exp_f32_e32 v102, v102
	v_exp_f32_e32 v118, v118
	v_exp_f32_e32 v103, v103
	v_exp_f32_e32 v119, v119
.Lfa0_join:
	v_exp_f32_e32 v106, v106
	v_exp_f32_e32 v122, v122
	v_exp_f32_e32 v107, v107
	v_exp_f32_e32 v123, v123
	v_exp_f32_e32 v110, v110
	v_exp_f32_e32 v126, v126
	v_exp_f32_e32 v111, v111
	v_exp_f32_e32 v127, v127
	v_cvt_pk_fp8_f32 v160, v96, v97
	v_cvt_pk_fp8_f32 v164, v112, v113
	v_cvt_pk_fp8_f32 v161, v100, v101
	v_cvt_pk_fp8_f32 v165, v116, v117
	v_cvt_pk_fp8_f32 v162, v104, v105
	v_cvt_pk_fp8_f32 v166, v120, v121
	v_cvt_pk_fp8_f32 v163, v108, v109
	v_cvt_pk_fp8_f32 v167, v124, v125
	v_cvt_pk_fp8_f32 v160, v98, v99 op_sel:[0,0,1]
	v_cvt_pk_fp8_f32 v164, v114, v115 op_sel:[0,0,1]
	v_cvt_pk_fp8_f32 v161, v102, v103 op_sel:[0,0,1]
	v_cvt_pk_fp8_f32 v165, v118, v119 op_sel:[0,0,1]
	v_cvt_pk_fp8_f32 v162, v106, v107 op_sel:[0,0,1]
	v_cvt_pk_fp8_f32 v166, v122, v123 op_sel:[0,0,1]
	v_cvt_pk_fp8_f32 v163, v110, v111 op_sel:[0,0,1]
	v_cvt_pk_fp8_f32 v167, v126, v127 op_sel:[0,0,1]
	s_waitcnt vmcnt(4)
	s_waitcnt lgkmcnt(0)
	s_barrier
	s_mov_b32 s13, s12
	s_add_i32 s12, s12, 1
	s_and_b32 s12, s12, 3
	s_add_i32 s2, s2, 1
	s_add_i32 s3, s3, 64
	s_cmp_lt_u32 s2, s16
	s_cbranch_scc1 .Lfa0_loop
	s_branch .LBB0_528
.Lfa0_rare:
	s_waitcnt lgkmcnt(4)
	v_mfma_scale_f32_32x32x64_f8f6f4 v[48:63], v[160:167], v[168:175], v[48:63], v219, v219 op_sel_hi:[0,0,0]
	s_waitcnt lgkmcnt(2)
	v_mfma_scale_f32_32x32x64_f8f6f4 v[32:47], v[160:167], v[192:199], v[32:47], v219, v219 op_sel_hi:[0,0,0]
	s_waitcnt lgkmcnt(0)
	v_mfma_scale_f32_32x32x64_f8f6f4 v[16:31], v[160:167], v[184:191], v[16:31], v219, v219 op_sel_hi:[0,0,0]
	s_nop 15
	s_nop 7
	v_max_f32_e32 v80, v226, v226
	v_max_f32_e32 v82, 0, v80
	s_and_saveexec_b64 s[0:1], s[6:7]
	v_exp_f32_e64 v80, -v82
	s_nop 0
	ds_write_b32 v223, v80 offset:49152
	s_or_b64 exec, exec, s[0:1]
	v_add_u32_e32 v210, s78, v224
	s_waitcnt lgkmcnt(0)
	v_add_u32_e32 v244, 0xc000, v210
	v_add_u32_e32 v245, 0xc008, v210
	v_add_u32_e32 v246, 0xc020, v210
	v_add_u32_e32 v247, 0xc028, v210
	v_add_u32_e32 v248, 0xc040, v210
	v_add_u32_e32 v249, 0xc048, v210
	v_add_u32_e32 v206, 0xc060, v210
	v_add_u32_e32 v207, 0xc068, v210
	ds_read2_b32 v[228:229], v244 offset1:1
	ds_read2_b32 v[230:231], v245 offset1:1
	ds_read2_b32 v[236:237], v246 offset1:1
	ds_read2_b32 v[238:239], v247 offset1:1
	ds_read2_b32 v[240:241], v248 offset1:1
	ds_read2_b32 v[242:243], v249 offset1:1
	ds_read2_b32 v[244:245], v206 offset1:1
	ds_read2_b32 v[246:247], v207 offset1:1
	v_add_f32_e32 v225, v225, v82
	v_xor_b32_e32 v80, 0x80000000, v225
	v_pk_add_f32 v[96:97], v[96:97], v[82:83] op_sel_hi:[1,0] neg_lo:[0,1] neg_hi:[0,1]
	v_pk_add_f32 v[112:113], v[112:113], v[82:83] op_sel_hi:[1,0] neg_lo:[0,1] neg_hi:[0,1]
	v_pk_add_f32 v[98:99], v[98:99], v[82:83] op_sel_hi:[1,0] neg_lo:[0,1] neg_hi:[0,1]
	v_pk_add_f32 v[114:115], v[114:115], v[82:83] op_sel_hi:[1,0] neg_lo:[0,1] neg_hi:[0,1]
	v_pk_add_f32 v[100:101], v[100:101], v[82:83] op_sel_hi:[1,0] neg_lo:[0,1] neg_hi:[0,1]
	v_pk_add_f32 v[116:117], v[116:117], v[82:83] op_sel_hi:[1,0] neg_lo:[0,1] neg_hi:[0,1]
	v_pk_add_f32 v[102:103], v[102:103], v[82:83] op_sel_hi:[1,0] neg_lo:[0,1] neg_hi:[0,1]
	v_pk_add_f32 v[118:119], v[118:119], v[82:83] op_sel_hi:[1,0] neg_lo:[0,1] neg_hi:[0,1]
	v_pk_add_f32 v[104:105], v[104:105], v[82:83] op_sel_hi:[1,0] neg_lo:[0,1] neg_hi:[0,1]
	v_pk_add_f32 v[120:121], v[120:121], v[82:83] op_sel_hi:[1,0] neg_lo:[0,1] neg_hi:[0,1]
	v_pk_add_f32 v[106:107], v[106:107], v[82:83] op_sel_hi:[1,0] neg_lo:[0,1] neg_hi:[0,1]
	v_pk_add_f32 v[122:123], v[122:123], v[82:83] op_sel_hi:[1,0] neg_lo:[0,1] neg_hi:[0,1]
	v_pk_add_f32 v[108:109], v[108:109], v[82:83] op_sel_hi:[1,0] neg_lo:[0,1] neg_hi:[0,1]
	v_pk_add_f32 v[124:125], v[124:125], v[82:83] op_sel_hi:[1,0] neg_lo:[0,1] neg_hi:[0,1]
	v_pk_add_f32 v[110:111], v[110:111], v[82:83] op_sel_hi:[1,0] neg_lo:[0,1] neg_hi:[0,1]
	v_pk_add_f32 v[126:127], v[126:127], v[82:83] op_sel_hi:[1,0] neg_lo:[0,1] neg_hi:[0,1]
	v_mov_b32_e32 v81, v80
	v_mov_b32_e32 v82, v80
	v_mov_b32_e32 v83, v80
	v_mov_b32_e32 v84, v80
	v_mov_b32_e32 v85, v80
	v_mov_b32_e32 v86, v80
	v_mov_b32_e32 v87, v80
	v_mov_b32_e32 v88, v80
	v_mov_b32_e32 v89, v80
	v_mov_b32_e32 v90, v80
	v_mov_b32_e32 v91, v80
	v_mov_b32_e32 v92, v80
	v_mov_b32_e32 v93, v80
	v_mov_b32_e32 v94, v80
	v_mov_b32_e32 v95, v80
	s_waitcnt lgkmcnt(0)
	v_pk_mul_f32 v[64:65], v[64:65], v[228:229]
	v_pk_mul_f32 v[66:67], v[66:67], v[230:231]
	v_pk_mul_f32 v[68:69], v[68:69], v[236:237]
	v_pk_mul_f32 v[70:71], v[70:71], v[238:239]
	v_pk_mul_f32 v[72:73], v[72:73], v[240:241]
	v_pk_mul_f32 v[74:75], v[74:75], v[242:243]
	v_pk_mul_f32 v[76:77], v[76:77], v[244:245]
	v_pk_mul_f32 v[78:79], v[78:79], v[246:247]
	v_pk_mul_f32 v[48:49], v[48:49], v[228:229]
	v_pk_mul_f32 v[50:51], v[50:51], v[230:231]
	v_pk_mul_f32 v[52:53], v[52:53], v[236:237]
	v_pk_mul_f32 v[54:55], v[54:55], v[238:239]
	v_pk_mul_f32 v[56:57], v[56:57], v[240:241]
	v_pk_mul_f32 v[58:59], v[58:59], v[242:243]
	v_pk_mul_f32 v[60:61], v[60:61], v[244:245]
	v_pk_mul_f32 v[62:63], v[62:63], v[246:247]
	v_pk_mul_f32 v[32:33], v[32:33], v[228:229]
	v_pk_mul_f32 v[34:35], v[34:35], v[230:231]
	v_pk_mul_f32 v[36:37], v[36:37], v[236:237]
	v_pk_mul_f32 v[38:39], v[38:39], v[238:239]
	v_pk_mul_f32 v[40:41], v[40:41], v[240:241]
	v_pk_mul_f32 v[42:43], v[42:43], v[242:243]
	v_pk_mul_f32 v[44:45], v[44:45], v[244:245]
	v_pk_mul_f32 v[46:47], v[46:47], v[246:247]
	v_pk_mul_f32 v[16:17], v[16:17], v[228:229]
	v_pk_mul_f32 v[18:19], v[18:19], v[230:231]
	v_pk_mul_f32 v[20:21], v[20:21], v[236:237]
	v_pk_mul_f32 v[22:23], v[22:23], v[238:239]
	v_pk_mul_f32 v[24:25], v[24:25], v[240:241]
	v_pk_mul_f32 v[26:27], v[26:27], v[242:243]
	v_pk_mul_f32 v[28:29], v[28:29], v[244:245]
	v_pk_mul_f32 v[30:31], v[30:31], v[246:247]
	v_pk_mul_f32 v[0:1], v[0:1], v[228:229]
	v_pk_mul_f32 v[2:3], v[2:3], v[230:231]
	v_pk_mul_f32 v[4:5], v[4:5], v[236:237]
	v_pk_mul_f32 v[6:7], v[6:7], v[238:239]
	v_pk_mul_f32 v[8:9], v[8:9], v[240:241]
	v_pk_mul_f32 v[10:11], v[10:11], v[242:243]
	v_pk_mul_f32 v[12:13], v[12:13], v[244:245]
	v_pk_mul_f32 v[14:15], v[14:15], v[246:247]
	v_exp_f32_e32 v96, v96
	v_exp_f32_e32 v112, v112
	v_exp_f32_e32 v97, v97
	v_exp_f32_e32 v113, v113
	v_exp_f32_e32 v100, v100
	v_exp_f32_e32 v116, v116
	v_exp_f32_e32 v101, v101
	v_exp_f32_e32 v117, v117
	v_exp_f32_e32 v104, v104
	v_exp_f32_e32 v120, v120
	v_exp_f32_e32 v105, v105
	v_exp_f32_e32 v121, v121
	v_exp_f32_e32 v108, v108
	v_exp_f32_e32 v124, v124
	v_exp_f32_e32 v109, v109
	v_exp_f32_e32 v125, v125
	v_exp_f32_e32 v98, v98
	v_exp_f32_e32 v114, v114
	v_exp_f32_e32 v99, v99
	v_exp_f32_e32 v115, v115
	v_exp_f32_e32 v102, v102
	v_exp_f32_e32 v118, v118
	v_exp_f32_e32 v103, v103
	v_exp_f32_e32 v119, v119
	s_branch .Lfa0_join
.Lfa1_entry:
	v_max3_f32 v226, v96, v97, v98
	v_max3_f32 v202, v99, v100, v101
	v_max3_f32 v203, v102, v103, v104
	v_max3_f32 v211, v105, v106, v107
	v_max3_f32 v226, v226, v108, v109
	v_max3_f32 v202, v202, v110, v111
	v_max3_f32 v226, v226, v203, v211
	v_max_f32_e32 v226, v226, v202
	v_max3_f32 v227, v112, v113, v114
	v_max3_f32 v202, v115, v116, v117
	v_max3_f32 v203, v118, v119, v120
	v_max3_f32 v211, v121, v122, v123
	v_max3_f32 v227, v227, v124, v125
	v_max3_f32 v202, v202, v126, v127
	v_max3_f32 v227, v227, v203, v211
	v_max_f32_e32 v227, v227, v202
	v_max_f32_e32 v226, v226, v227
	v_mov_b32_e32 v227, v226
	s_nop 1
	v_permlane32_swap_b32_e32 v226, v227
	v_max3_f32 v226, v226, v227, v227
	s_nop 0
	v_cmp_lt_f32_e32 vcc, 0x41000000, v226
	s_cbranch_vccz .Lfa1_entry_exp
	v_max_f32_e32 v80, v226, v226
	v_max_f32_e32 v82, 0, v80
	s_and_saveexec_b64 s[0:1], s[6:7]
	v_exp_f32_e64 v80, -v82
	s_nop 0
	ds_write_b32 v223, v80 offset:49152
	s_or_b64 exec, exec, s[0:1]
	v_add_u32_e32 v210, s78, v224
	s_waitcnt lgkmcnt(0)
	v_add_u32_e32 v244, 0xc000, v210
	v_add_u32_e32 v245, 0xc008, v210
	v_add_u32_e32 v246, 0xc020, v210
	v_add_u32_e32 v247, 0xc028, v210
	v_add_u32_e32 v248, 0xc040, v210
	v_add_u32_e32 v249, 0xc048, v210
	v_add_u32_e32 v206, 0xc060, v210
	v_add_u32_e32 v207, 0xc068, v210
	ds_read2_b32 v[228:229], v244 offset1:1
	ds_read2_b32 v[230:231], v245 offset1:1
	ds_read2_b32 v[236:237], v246 offset1:1
	ds_read2_b32 v[238:239], v247 offset1:1
	ds_read2_b32 v[240:241], v248 offset1:1
	ds_read2_b32 v[242:243], v249 offset1:1
	ds_read2_b32 v[244:245], v206 offset1:1
	ds_read2_b32 v[246:247], v207 offset1:1
	v_add_f32_e32 v225, v225, v82
	v_xor_b32_e32 v80, 0x80000000, v225
	v_pk_add_f32 v[96:97], v[96:97], v[82:83] op_sel_hi:[1,0] neg_lo:[0,1] neg_hi:[0,1]
	v_pk_add_f32 v[112:113], v[112:113], v[82:83] op_sel_hi:[1,0] neg_lo:[0,1] neg_hi:[0,1]
	v_pk_add_f32 v[98:99], v[98:99], v[82:83] op_sel_hi:[1,0] neg_lo:[0,1] neg_hi:[0,1]
	v_pk_add_f32 v[114:115], v[114:115], v[82:83] op_sel_hi:[1,0] neg_lo:[0,1] neg_hi:[0,1]
	v_pk_add_f32 v[100:101], v[100:101], v[82:83] op_sel_hi:[1,0] neg_lo:[0,1] neg_hi:[0,1]
	v_pk_add_f32 v[116:117], v[116:117], v[82:83] op_sel_hi:[1,0] neg_lo:[0,1] neg_hi:[0,1]
	v_pk_add_f32 v[102:103], v[102:103], v[82:83] op_sel_hi:[1,0] neg_lo:[0,1] neg_hi:[0,1]
	v_pk_add_f32 v[118:119], v[118:119], v[82:83] op_sel_hi:[1,0] neg_lo:[0,1] neg_hi:[0,1]
	v_pk_add_f32 v[104:105], v[104:105], v[82:83] op_sel_hi:[1,0] neg_lo:[0,1] neg_hi:[0,1]
	v_pk_add_f32 v[120:121], v[120:121], v[82:83] op_sel_hi:[1,0] neg_lo:[0,1] neg_hi:[0,1]
	v_pk_add_f32 v[106:107], v[106:107], v[82:83] op_sel_hi:[1,0] neg_lo:[0,1] neg_hi:[0,1]
	v_pk_add_f32 v[122:123], v[122:123], v[82:83] op_sel_hi:[1,0] neg_lo:[0,1] neg_hi:[0,1]
	v_pk_add_f32 v[108:109], v[108:109], v[82:83] op_sel_hi:[1,0] neg_lo:[0,1] neg_hi:[0,1]
	v_pk_add_f32 v[124:125], v[124:125], v[82:83] op_sel_hi:[1,0] neg_lo:[0,1] neg_hi:[0,1]
	v_pk_add_f32 v[110:111], v[110:111], v[82:83] op_sel_hi:[1,0] neg_lo:[0,1] neg_hi:[0,1]
	v_pk_add_f32 v[126:127], v[126:127], v[82:83] op_sel_hi:[1,0] neg_lo:[0,1] neg_hi:[0,1]
	v_mov_b32_e32 v81, v80
	v_mov_b32_e32 v82, v80
	v_mov_b32_e32 v83, v80
	v_mov_b32_e32 v84, v80
	v_mov_b32_e32 v85, v80
	v_mov_b32_e32 v86, v80
	v_mov_b32_e32 v87, v80
	v_mov_b32_e32 v88, v80
	v_mov_b32_e32 v89, v80
	v_mov_b32_e32 v90, v80
	v_mov_b32_e32 v91, v80
	v_mov_b32_e32 v92, v80
	v_mov_b32_e32 v93, v80
	v_mov_b32_e32 v94, v80
	v_mov_b32_e32 v95, v80
	s_waitcnt lgkmcnt(0)
	v_pk_mul_f32 v[64:65], v[64:65], v[228:229]
	v_pk_mul_f32 v[66:67], v[66:67], v[230:231]
	v_pk_mul_f32 v[68:69], v[68:69], v[236:237]
	v_pk_mul_f32 v[70:71], v[70:71], v[238:239]
	v_pk_mul_f32 v[72:73], v[72:73], v[240:241]
	v_pk_mul_f32 v[74:75], v[74:75], v[242:243]
	v_pk_mul_f32 v[76:77], v[76:77], v[244:245]
	v_pk_mul_f32 v[78:79], v[78:79], v[246:247]
	v_pk_mul_f32 v[48:49], v[48:49], v[228:229]
	v_pk_mul_f32 v[50:51], v[50:51], v[230:231]
	v_pk_mul_f32 v[52:53], v[52:53], v[236:237]
	v_pk_mul_f32 v[54:55], v[54:55], v[238:239]
	v_pk_mul_f32 v[56:57], v[56:57], v[240:241]
	v_pk_mul_f32 v[58:59], v[58:59], v[242:243]
	v_pk_mul_f32 v[60:61], v[60:61], v[244:245]
	v_pk_mul_f32 v[62:63], v[62:63], v[246:247]
	v_pk_mul_f32 v[32:33], v[32:33], v[228:229]
	v_pk_mul_f32 v[34:35], v[34:35], v[230:231]
	v_pk_mul_f32 v[36:37], v[36:37], v[236:237]
	v_pk_mul_f32 v[38:39], v[38:39], v[238:239]
	v_pk_mul_f32 v[40:41], v[40:41], v[240:241]
	v_pk_mul_f32 v[42:43], v[42:43], v[242:243]
	v_pk_mul_f32 v[44:45], v[44:45], v[244:245]
	v_pk_mul_f32 v[46:47], v[46:47], v[246:247]
	v_pk_mul_f32 v[16:17], v[16:17], v[228:229]
	v_pk_mul_f32 v[18:19], v[18:19], v[230:231]
	v_pk_mul_f32 v[20:21], v[20:21], v[236:237]
	v_pk_mul_f32 v[22:23], v[22:23], v[238:239]
	v_pk_mul_f32 v[24:25], v[24:25], v[240:241]
	v_pk_mul_f32 v[26:27], v[26:27], v[242:243]
	v_pk_mul_f32 v[28:29], v[28:29], v[244:245]
	v_pk_mul_f32 v[30:31], v[30:31], v[246:247]
	v_pk_mul_f32 v[0:1], v[0:1], v[228:229]
	v_pk_mul_f32 v[2:3], v[2:3], v[230:231]
	v_pk_mul_f32 v[4:5], v[4:5], v[236:237]
	v_pk_mul_f32 v[6:7], v[6:7], v[238:239]
	v_pk_mul_f32 v[8:9], v[8:9], v[240:241]
	v_pk_mul_f32 v[10:11], v[10:11], v[242:243]
	v_pk_mul_f32 v[12:13], v[12:13], v[244:245]
	v_pk_mul_f32 v[14:15], v[14:15], v[246:247]
.Lfa1_entry_exp:
	v_exp_f32_e32 v96, v96
	v_exp_f32_e32 v112, v112
	v_exp_f32_e32 v97, v97
	v_exp_f32_e32 v113, v113
	v_exp_f32_e32 v100, v100
	v_exp_f32_e32 v116, v116
	v_exp_f32_e32 v101, v101
	v_exp_f32_e32 v117, v117
	v_exp_f32_e32 v104, v104
	v_exp_f32_e32 v120, v120
	v_exp_f32_e32 v105, v105
	v_exp_f32_e32 v121, v121
	v_exp_f32_e32 v108, v108
	v_exp_f32_e32 v124, v124
	v_exp_f32_e32 v109, v109
	v_exp_f32_e32 v125, v125
	v_exp_f32_e32 v98, v98
	v_exp_f32_e32 v114, v114
	v_exp_f32_e32 v99, v99
	v_exp_f32_e32 v115, v115
	v_exp_f32_e32 v102, v102
	v_exp_f32_e32 v118, v118
	v_exp_f32_e32 v103, v103
	v_exp_f32_e32 v119, v119
.Lfa1_loop:
	s_add_i32 s10, s12, 3
	s_and_b32 s10, s10, 3
	s_add_i32 s33, s10, 3
	s_and_b32 s33, s33, 3
	s_lshl_b32 s33, s33, 13
	s_add_i32 s33, s33, s79
	s_addk_i32 s33, 0x4000
	s_add_i32 s32, s86, s2
	s_add_i32 s50, s32, -1
	s_mov_b32 s51, 0
	s_lshl_b64 s[50:51], s[50:51], 6
	s_add_u32 s50, s97, s50
	s_addc_u32 s51, s87, s51
	s_mov_b32 m0, s33
	s_nop 0
	global_load_lds_dwordx4 v218, s[50:51]
	s_lshl_b32 s0, s12, 12
	s_add_i32 s0, s91, s0
	s_lshl_b32 s1, s13, 13
	s_add_i32 s1, s91, s1
	v_add_u32_e32 v232, s0, v222
	v_add_u32_e32 v233, s0, v221
	v_add_u32_e32 v234, s1, v222
	v_add_u32_e32 v235, s1, v221
	ds_read_b128 v[144:147], v232
	ds_read_b128 v[148:151], v233
	ds_read_b128 v[152:155], v232 offset:2048
	ds_read_b128 v[156:159], v233 offset:2048
	ds_read_b128 v[176:179], v234 offset:16384
	ds_read_b128 v[180:183], v235 offset:16384
	ds_read_b128 v[168:171], v234 offset:18432
	ds_read_b128 v[172:175], v235 offset:18432
	ds_read_b128 v[192:195], v234 offset:20480
	ds_read_b128 v[196:199], v235 offset:20480
	ds_read_b128 v[184:187], v234 offset:22528
	ds_read_b128 v[188:191], v235 offset:22528
	v_exp_f32_e32 v106, v106
	v_exp_f32_e32 v122, v122
	v_exp_f32_e32 v107, v107
	v_exp_f32_e32 v123, v123
	v_exp_f32_e32 v110, v110
	v_exp_f32_e32 v126, v126
	v_exp_f32_e32 v111, v111
	v_exp_f32_e32 v127, v127
	v_cvt_pk_fp8_f32 v160, v96, v97
	v_cvt_pk_fp8_f32 v164, v112, v113
	v_cvt_pk_fp8_f32 v161, v100, v101
	v_cvt_pk_fp8_f32 v165, v116, v117
	v_cvt_pk_fp8_f32 v162, v104, v105
	v_cvt_pk_fp8_f32 v166, v120, v121
	v_cvt_pk_fp8_f32 v163, v108, v109
	v_cvt_pk_fp8_f32 v167, v124, v125
	v_cvt_pk_fp8_f32 v160, v98, v99 op_sel:[0,0,1]
	v_cvt_pk_fp8_f32 v164, v114, v115 op_sel:[0,0,1]
	v_cvt_pk_fp8_f32 v161, v102, v103 op_sel:[0,0,1]
	v_cvt_pk_fp8_f32 v165, v118, v119 op_sel:[0,0,1]
	v_cvt_pk_fp8_f32 v162, v106, v107 op_sel:[0,0,1]
	v_cvt_pk_fp8_f32 v166, v122, v123 op_sel:[0,0,1]
	v_cvt_pk_fp8_f32 v163, v110, v111 op_sel:[0,0,1]
	v_cvt_pk_fp8_f32 v167, v126, v127 op_sel:[0,0,1]
	s_waitcnt lgkmcnt(10)
	v_mfma_scale_f32_32x32x64_f8f6f4 v[96:111], v[144:151], v[128:135], v[80:95], v220, v220 op_sel_hi:[0,0,0]
	s_waitcnt lgkmcnt(8)
	v_mfma_scale_f32_32x32x64_f8f6f4 v[112:127], v[152:159], v[128:135], v[80:95], v220, v220 op_sel_hi:[0,0,0]
	v_mfma_scale_f32_32x32x64_f8f6f4 v[0:15], v[160:167], v[136:143], v[0:15], v219, v219 op_sel_hi:[0,0,0]
	v_max3_f32 v226, v96, v97, v98
	v_max3_f32 v202, v99, v100, v101
	v_max3_f32 v203, v102, v103, v104
	v_max3_f32 v211, v105, v106, v107
	v_max3_f32 v226, v226, v108, v109
	v_max3_f32 v202, v202, v110, v111
	v_max3_f32 v226, v226, v203, v211
	v_max_f32_e32 v226, v226, v202
	s_waitcnt lgkmcnt(6)
	v_mfma_scale_f32_32x32x64_f8f6f4 v[64:79], v[160:167], v[176:183], v[64:79], v219, v219 op_sel_hi:[0,0,0]
	v_max3_f32 v227, v112, v113, v114
	v_max3_f32 v202, v115, v116, v117
	v_max3_f32 v203, v118, v119, v120
	v_max3_f32 v211, v121, v122, v123
	v_max3_f32 v227, v227, v124, v125
	v_max3_f32 v202, v202, v126, v127
	v_max3_f32 v227, v227, v203, v211
	v_max_f32_e32 v227, v227, v202
	v_max_f32_e32 v226, v226, v227
	v_mov_b32_e32 v227, v226
	s_nop 1
	v_permlane32_swap_b32_e32 v226, v227
	v_max3_f32 v226, v226, v227, v227
	s_nop 0
	v_cmp_lt_f32_e32 vcc, 0x41000000, v226
	s_cbranch_vccnz .Lfa1_rare
	s_waitcnt lgkmcnt(4)
	v_mfma_scale_f32_32x32x64_f8f6f4 v[48:63], v[160:167], v[168:175], v[48:63], v219, v219 op_sel_hi:[0,0,0]
	v_exp_f32_e32 v96, v96
	v_exp_f32_e32 v112, v112
	v_exp_f32_e32 v97, v97
	v_exp_f32_e32 v113, v113
	v_exp_f32_e32 v100, v100
	v_exp_f32_e32 v116, v116
	v_exp_f32_e32 v101, v101
	v_exp_f32_e32 v117, v117
	s_waitcnt lgkmcnt(2)
	v_mfma_scale_f32_32x32x64_f8f6f4 v[32:47], v[160:167], v[192:199], v[32:47], v219, v219 op_sel_hi:[0,0,0]
	v_exp_f32_e32 v104, v104
	v_exp_f32_e32 v120, v120
	v_exp_f32_e32 v105, v105
	v_exp_f32_e32 v121, v121
	v_exp_f32_e32 v108, v108
	v_exp_f32_e32 v124, v124
	v_exp_f32_e32 v109, v109
	v_exp_f32_e32 v125, v125
	s_waitcnt lgkmcnt(0)
	v_mfma_scale_f32_32x32x64_f8f6f4 v[16:31], v[160:167], v[184:191], v[16:31], v219, v219 op_sel_hi:[0,0,0]
	v_exp_f32_e32 v98, v98
	v_exp_f32_e32 v114, v114
	v_exp_f32_e32 v99, v99
	v_exp_f32_e32 v115, v115
	v_exp_f32_e32 v102, v102
	v_exp_f32_e32 v118, v118
	v_exp_f32_e32 v103, v103
	v_exp_f32_e32 v119, v119
.Lfa1_join:
	s_waitcnt vmcnt(2)
	s_waitcnt lgkmcnt(0)
	s_barrier
	s_mov_b32 s13, s12
	s_add_i32 s12, s12, 1
	s_and_b32 s12, s12, 3
	s_add_i32 s2, s2, 1
	s_add_i32 s3, s3, 64
	s_cmp_lt_u32 s2, s16
	s_cbranch_scc1 .Lfa1_loop
	v_exp_f32_e32 v106, v106
	v_exp_f32_e32 v122, v122
	v_exp_f32_e32 v107, v107
	v_exp_f32_e32 v123, v123
	v_exp_f32_e32 v110, v110
	v_exp_f32_e32 v126, v126
	v_exp_f32_e32 v111, v111
	v_exp_f32_e32 v127, v127
	v_cvt_pk_fp8_f32 v160, v96, v97
	v_cvt_pk_fp8_f32 v164, v112, v113
	v_cvt_pk_fp8_f32 v161, v100, v101
	v_cvt_pk_fp8_f32 v165, v116, v117
	v_cvt_pk_fp8_f32 v162, v104, v105
	v_cvt_pk_fp8_f32 v166, v120, v121
	v_cvt_pk_fp8_f32 v163, v108, v109
	v_cvt_pk_fp8_f32 v167, v124, v125
	v_cvt_pk_fp8_f32 v160, v98, v99 op_sel:[0,0,1]
	v_cvt_pk_fp8_f32 v164, v114, v115 op_sel:[0,0,1]
	v_cvt_pk_fp8_f32 v161, v102, v103 op_sel:[0,0,1]
	v_cvt_pk_fp8_f32 v165, v118, v119 op_sel:[0,0,1]
	v_cvt_pk_fp8_f32 v162, v106, v107 op_sel:[0,0,1]
	v_cvt_pk_fp8_f32 v166, v122, v123 op_sel:[0,0,1]
	v_cvt_pk_fp8_f32 v163, v110, v111 op_sel:[0,0,1]
	v_cvt_pk_fp8_f32 v167, v126, v127 op_sel:[0,0,1]
	s_branch .LBB0_528
